# A5-A7: attention pass - no store drain before branch 2's K/V DMA nor at the top of a pass; selection-mask load issued before the Q fragment loads and waited with vmcnt(8) so the Q loads overlap the ma
# baseline (speedup 1.0000x reference)
.LBB0_828:
	s_and_b64 s[0:1], s[4:5], exec
	v_readlane_b32 s0, v255, 3
	v_readlane_b32 s1, v255, 4
	s_cselect_b32 s66, s1, s0
	v_mov_b32_e32 v2, v163
	s_lshl_b32 s0, s66, 6
	s_or_b32 s0, s0, s18
	v_and_b32_e32 v48, 31, v2
	v_or_b32_e32 v0, s0, v48
	v_readlane_b32 s0, v255, 21
	v_readlane_b32 s1, v255, 22
	v_ashrrev_i32_e32 v49, 5, v2
	v_lshlrev_b32_e32 v6, 3, v49
	v_mov_b64_e32 v[4:5], s[0:1]
	v_mad_i64_i32 v[4:5], s[0:1], v0, s67, v[4:5]
	v_ashrrev_i32_e32 v7, 31, v6
	v_readlane_b32 s0, v255, 5
	v_ashrrev_i32_e32 v1, 31, v0
	v_lshl_add_u64 v[4:5], v[6:7], 1, v[4:5]
	v_readlane_b32 s1, v255, 6
	s_nop 1
	v_lshl_add_u64 v[6:7], v[0:1], 3, s[0:1]
	global_load_dwordx2 v[182:183], v[6:7], off
	global_load_dwordx4 v[128:131], v[4:5], off offset:3072
	global_load_dwordx4 v[132:135], v[4:5], off offset:3104
	global_load_dwordx4 v[136:139], v[4:5], off offset:3136
	global_load_dwordx4 v[140:143], v[4:5], off offset:3168
	global_load_dwordx4 v[144:147], v[4:5], off offset:3200
	global_load_dwordx4 v[148:151], v[4:5], off offset:3232
	global_load_dwordx4 v[152:155], v[4:5], off offset:3264
	global_load_dwordx4 v[156:159], v[4:5], off offset:3296
	v_and_b32_e32 v3, 64, v199
	v_add_u32_e32 v5, 64, v3
	v_xor_b32_e32 v3, 1, v199
	v_cmp_lt_i32_e32 vcc, v3, v5
	v_xor_b32_e32 v6, 2, v199
	v_readlane_b32 s0, v254, 41
	v_cndmask_b32_e32 v3, v199, v3, vcc
	v_lshlrev_b32_e32 v3, 2, v3
	v_cmp_lt_i32_e32 vcc, v6, v5
	v_readlane_b32 s1, v254, 42
	s_waitcnt vmcnt(8)
	ds_bpermute_b32 v4, v3, v182
	ds_bpermute_b32 v3, v3, v183
	v_cndmask_b32_e32 v6, v199, v6, vcc
	v_lshlrev_b32_e32 v6, 2, v6
	s_waitcnt lgkmcnt(0)
	v_or_b32_e32 v4, v4, v182
	s_waitcnt lgkmcnt(0)
	v_or_b32_e32 v3, v3, v183
	ds_bpermute_b32 v7, v6, v4
	ds_bpermute_b32 v6, v6, v3
	s_waitcnt lgkmcnt(1)
	v_or_b32_e32 v4, v7, v4
	s_waitcnt lgkmcnt(0)
	v_or_b32_e32 v3, v6, v3
	v_xor_b32_e32 v6, 4, v199
	v_cmp_lt_i32_e32 vcc, v6, v5
	s_nop 1
	v_cndmask_b32_e32 v6, v199, v6, vcc
	v_lshlrev_b32_e32 v6, 2, v6
	ds_bpermute_b32 v7, v6, v4
	ds_bpermute_b32 v6, v6, v3
	s_waitcnt lgkmcnt(1)
	v_or_b32_e32 v4, v7, v4
	s_waitcnt lgkmcnt(0)
	v_or_b32_e32 v6, v6, v3
	v_xor_b32_e32 v3, 8, v199
	v_cmp_lt_i32_e32 vcc, v3, v5
	s_nop 1
	v_cndmask_b32_e32 v3, v199, v3, vcc
	v_lshlrev_b32_e32 v7, 2, v3
	ds_bpermute_b32 v3, v7, v4
	s_waitcnt lgkmcnt(0)
	v_or_b32_e32 v3, v3, v4
	ds_bpermute_b32 v4, v7, v6
	s_waitcnt lgkmcnt(0)
	v_or_b32_e32 v4, v4, v6
	v_xor_b32_e32 v6, 16, v199
	v_cmp_lt_i32_e32 vcc, v6, v5
	s_nop 1
	v_cndmask_b32_e32 v5, v199, v6, vcc
	v_lshlrev_b32_e32 v6, 2, v5
	ds_bpermute_b32 v5, v6, v3
	ds_bpermute_b32 v6, v6, v4
	v_cmp_eq_u32_e32 vcc, 0, v2
	s_and_b64 s[2:3], s[0:1], vcc
	s_and_saveexec_b64 s[0:1], s[2:3]
	s_cbranch_execz .LBB0_830
	v_readlane_b32 s2, v254, 43
	s_waitcnt lgkmcnt(0)
	v_or_b32_e32 v7, v6, v4
	v_or_b32_e32 v6, v5, v3
	v_mov_b32_e32 v3, s2
	ds_write_b64 v3, v[6:7]

.LBB0_880:
	s_waitcnt vmcnt(0)
	v_add_f32_e32 v0, v160, v164
	v_mul_f32_e32 v0, 0xbfb8aa3b, v0
	v_exp_f32_e32 v0, v0
	s_max_i32 s2, s66, 8
	s_add_i32 s2, s2, -8
	v_readlane_b32 s74, v255, 23
	s_lshl_b64 s[2:3], -1, s2
	v_readlane_b32 s75, v255, 24
	v_add_f32_e32 v0, 1.0, v0
	s_and_b64 s[2:3], s[74:75], s[2:3]
	v_div_scale_f32 v1, s[74:75], v0, v0, 1.0
	v_rcp_f32_e32 v2, v1
	v_lshlrev_b64 v[8:9], 2, v[174:175]
	s_waitcnt vmcnt(0)
	v_fma_f32 v3, -v1, v2, 1.0
	v_fmac_f32_e32 v2, v3, v2
	v_div_scale_f32 v3, vcc, 1.0, v0, 1.0
	v_mul_f32_e32 v4, v3, v2
	v_fma_f32 v5, -v1, v4, v3
	v_fmac_f32_e32 v4, v5, v2
	v_fma_f32 v1, -v1, v4, v3
	v_div_fmas_f32 v1, v1, v2, v4
	v_div_fixup_f32 v4, v1, v0, 1.0
	v_add_f32_e32 v0, v161, v165
	v_mul_f32_e32 v0, 0xbfb8aa3b, v0
	v_exp_f32_e32 v0, v0
	s_barrier
	s_ff1_i32_b64 s94, s[2:3]
	v_add_f32_e32 v0, 1.0, v0
	v_div_scale_f32 v1, s[74:75], v0, v0, 1.0
	v_rcp_f32_e32 v2, v1
	v_readlane_b32 s74, v255, 9
	v_readlane_b32 s75, v255, 10
	s_mul_i32 s67, s94, 0xc8000
	v_fma_f32 v3, -v1, v2, 1.0
	v_fmac_f32_e32 v2, v3, v2
	v_div_scale_f32 v3, vcc, 1.0, v0, 1.0
	v_mul_f32_e32 v5, v3, v2
	v_fma_f32 v6, -v1, v5, v3
	v_fmac_f32_e32 v5, v6, v2
	v_fma_f32 v1, -v1, v5, v3
	v_div_fmas_f32 v1, v1, v2, v5
	v_div_fixup_f32 v6, v1, v0, 1.0
	v_lshlrev_b64 v[0:1], 2, v[184:185]
	v_lshl_add_u64 v[2:3], s[74:75], 0, v[0:1]
	v_readlane_b32 s74, v255, 11
	v_readlane_b32 s75, v255, 12
	v_lshl_add_u64 v[10:11], v[2:3], 0, v[8:9]
	v_readlane_b32 s68, v255, 13
	v_lshl_add_u64 v[0:1], s[74:75], 0, v[0:1]
	v_lshl_add_u64 v[160:161], v[0:1], 0, v[8:9]
	v_mov_b32_e32 v0, v228
	s_nop 1
	v_permlane32_swap_b32_e32 v228, v0
	v_add_f32_e32 v0, v228, v0
	v_div_scale_f32 v1, s[74:75], v0, v0, 1.0
	v_rcp_f32_e32 v2, v1
	s_add_u32 s74, s2, -1
	s_addc_u32 s75, s3, -1
	s_and_b64 s[2:3], s[74:75], s[2:3]
	v_fma_f32 v3, -v1, v2, 1.0
	v_fmac_f32_e32 v2, v3, v2
	v_div_scale_f32 v3, vcc, 1.0, v0, 1.0
	v_mul_f32_e32 v5, v3, v2
	v_fma_f32 v7, -v1, v5, v3
	v_fmac_f32_e32 v5, v7, v2
	v_fma_f32 v1, -v1, v5, v3
	v_div_fmas_f32 v1, v1, v2, v5
	v_div_fixup_f32 v8, v1, v0, 1.0
	global_load_dwordx4 v[64:67], v[10:11], off
	global_load_dwordx4 v[68:71], v[10:11], off offset:32
	global_load_dwordx4 v[72:75], v[10:11], off offset:64
	global_load_dwordx4 v[76:79], v[10:11], off offset:96
	global_load_dwordx4 v[96:99], v[10:11], off offset:128
	global_load_dwordx4 v[100:103], v[10:11], off offset:160
	global_load_dwordx4 v[104:107], v[10:11], off offset:192
	global_load_dwordx4 v[108:111], v[10:11], off offset:224
	global_load_dwordx4 v[112:115], v[10:11], off offset:256
	global_load_dwordx4 v[116:119], v[10:11], off offset:288
	global_load_dwordx4 v[120:123], v[10:11], off offset:320
	global_load_dwordx4 v[124:127], v[10:11], off offset:352
	global_load_dwordx4 v[228:231], v[10:11], off offset:384
	global_load_dwordx4 v[232:235], v[10:11], off offset:416
	global_load_dwordx4 v[236:239], v[10:11], off offset:448
	global_load_dwordx4 v[240:243], v[10:11], off offset:480
	v_pk_mul_f32 v[12:13], v[80:81], v[8:9] op_sel_hi:[1,0]
	s_add_u32 s74, s68, s67
	v_pk_mul_f32 v[12:13], v[6:7], v[12:13] op_sel_hi:[0,1]
	v_readlane_b32 s67, v255, 14
	s_addc_u32 s75, s67, 0
	s_lshl_b32 s67, s94, 7
	v_readlane_b32 s68, v255, 15
	s_add_u32 vcc_lo, s68, s67
	v_readlane_b32 s67, v255, 16
	s_addc_u32 vcc_hi, s67, 0
	s_mov_b32 m0, s69
	v_readlane_b32 s67, v255, 25
	s_cmp_eq_u64 s[2:3], 0
	s_ff1_i32_b64 s84, s[2:3]
	s_waitcnt vmcnt(15)
	v_pk_fma_f32 v[64:65], v[4:5], v[64:65], v[12:13] op_sel_hi:[0,1,1]
	v_pk_mul_f32 v[12:13], v[82:83], v[8:9] op_sel_hi:[1,0]
	s_nop 0
	v_pk_mul_f32 v[12:13], v[6:7], v[12:13] op_sel_hi:[0,1]
	v_pk_fma_f32 v[66:67], v[4:5], v[66:67], v[12:13] op_sel_hi:[0,1,1]
	global_store_dwordx4 v[160:161], v[64:67], off
	v_pk_mul_f32 v[12:13], v[84:85], v[8:9] op_sel_hi:[1,0]
	s_waitcnt vmcnt(15)
	v_pk_mul_f32 v[68:69], v[4:5], v[68:69] op_sel_hi:[0,1]
	v_pk_fma_f32 v[68:69], v[6:7], v[12:13], v[68:69] op_sel_hi:[0,1,1]
	v_pk_mul_f32 v[12:13], v[86:87], v[8:9] op_sel_hi:[1,0]
	v_pk_mul_f32 v[70:71], v[4:5], v[70:71] op_sel_hi:[0,1]
	v_pk_fma_f32 v[70:71], v[6:7], v[12:13], v[70:71] op_sel_hi:[0,1,1]
	global_store_dwordx4 v[160:161], v[68:71], off offset:32
	v_pk_mul_f32 v[12:13], v[88:89], v[8:9] op_sel_hi:[1,0]
	s_waitcnt vmcnt(15)
	v_pk_mul_f32 v[72:73], v[4:5], v[72:73] op_sel_hi:[0,1]
	v_pk_fma_f32 v[72:73], v[6:7], v[12:13], v[72:73] op_sel_hi:[0,1,1]
	v_pk_mul_f32 v[12:13], v[90:91], v[8:9] op_sel_hi:[1,0]
	v_pk_mul_f32 v[74:75], v[4:5], v[74:75] op_sel_hi:[0,1]
	v_pk_fma_f32 v[74:75], v[6:7], v[12:13], v[74:75] op_sel_hi:[0,1,1]
	global_store_dwordx4 v[160:161], v[72:75], off offset:64
	v_pk_mul_f32 v[12:13], v[92:93], v[8:9] op_sel_hi:[1,0]
	s_waitcnt vmcnt(15)
	v_pk_mul_f32 v[76:77], v[4:5], v[76:77] op_sel_hi:[0,1]
	v_pk_fma_f32 v[76:77], v[6:7], v[12:13], v[76:77] op_sel_hi:[0,1,1]
	v_pk_mul_f32 v[12:13], v[94:95], v[8:9] op_sel_hi:[1,0]
	v_pk_mul_f32 v[78:79], v[4:5], v[78:79] op_sel_hi:[0,1]
	v_pk_fma_f32 v[78:79], v[6:7], v[12:13], v[78:79] op_sel_hi:[0,1,1]
	global_store_dwordx4 v[160:161], v[76:79], off offset:96
	v_pk_mul_f32 v[12:13], v[48:49], v[8:9] op_sel_hi:[1,0]
	s_waitcnt vmcnt(15)
	v_pk_mul_f32 v[96:97], v[4:5], v[96:97] op_sel_hi:[0,1]
	v_pk_fma_f32 v[96:97], v[6:7], v[12:13], v[96:97] op_sel_hi:[0,1,1]
	v_pk_mul_f32 v[12:13], v[50:51], v[8:9] op_sel_hi:[1,0]
	v_pk_mul_f32 v[98:99], v[4:5], v[98:99] op_sel_hi:[0,1]
	v_pk_fma_f32 v[98:99], v[6:7], v[12:13], v[98:99] op_sel_hi:[0,1,1]
	global_store_dwordx4 v[160:161], v[96:99], off offset:128
	v_pk_mul_f32 v[12:13], v[52:53], v[8:9] op_sel_hi:[1,0]
	s_waitcnt vmcnt(15)
	v_pk_mul_f32 v[100:101], v[4:5], v[100:101] op_sel_hi:[0,1]
	v_pk_fma_f32 v[100:101], v[6:7], v[12:13], v[100:101] op_sel_hi:[0,1,1]
	v_pk_mul_f32 v[12:13], v[54:55], v[8:9] op_sel_hi:[1,0]
	v_pk_mul_f32 v[102:103], v[4:5], v[102:103] op_sel_hi:[0,1]
	v_pk_fma_f32 v[102:103], v[6:7], v[12:13], v[102:103] op_sel_hi:[0,1,1]
	global_store_dwordx4 v[160:161], v[100:103], off offset:160
	v_pk_mul_f32 v[12:13], v[56:57], v[8:9] op_sel_hi:[1,0]
	s_waitcnt vmcnt(15)
	v_pk_mul_f32 v[104:105], v[4:5], v[104:105] op_sel_hi:[0,1]
	v_pk_fma_f32 v[104:105], v[6:7], v[12:13], v[104:105] op_sel_hi:[0,1,1]
	v_pk_mul_f32 v[12:13], v[58:59], v[8:9] op_sel_hi:[1,0]
	v_pk_mul_f32 v[106:107], v[4:5], v[106:107] op_sel_hi:[0,1]
	v_pk_fma_f32 v[106:107], v[6:7], v[12:13], v[106:107] op_sel_hi:[0,1,1]
	global_store_dwordx4 v[160:161], v[104:107], off offset:192
	v_pk_mul_f32 v[12:13], v[60:61], v[8:9] op_sel_hi:[1,0]
	s_waitcnt vmcnt(15)
	v_pk_mul_f32 v[108:109], v[4:5], v[108:109] op_sel_hi:[0,1]
	v_pk_fma_f32 v[108:109], v[6:7], v[12:13], v[108:109] op_sel_hi:[0,1,1]
	v_pk_mul_f32 v[12:13], v[62:63], v[8:9] op_sel_hi:[1,0]
	v_pk_mul_f32 v[110:111], v[4:5], v[110:111] op_sel_hi:[0,1]
	v_pk_fma_f32 v[110:111], v[6:7], v[12:13], v[110:111] op_sel_hi:[0,1,1]
	global_store_dwordx4 v[160:161], v[108:111], off offset:224
	v_pk_mul_f32 v[12:13], v[32:33], v[8:9] op_sel_hi:[1,0]
	s_waitcnt vmcnt(15)
	v_pk_mul_f32 v[112:113], v[4:5], v[112:113] op_sel_hi:[0,1]
	v_pk_fma_f32 v[112:113], v[6:7], v[12:13], v[112:113] op_sel_hi:[0,1,1]
	v_pk_mul_f32 v[12:13], v[34:35], v[8:9] op_sel_hi:[1,0]
	v_pk_mul_f32 v[114:115], v[4:5], v[114:115] op_sel_hi:[0,1]
	v_pk_fma_f32 v[114:115], v[6:7], v[12:13], v[114:115] op_sel_hi:[0,1,1]
	global_store_dwordx4 v[160:161], v[112:115], off offset:256
	v_pk_mul_f32 v[12:13], v[36:37], v[8:9] op_sel_hi:[1,0]
	s_waitcnt vmcnt(15)
	v_pk_mul_f32 v[116:117], v[4:5], v[116:117] op_sel_hi:[0,1]
	v_pk_fma_f32 v[116:117], v[6:7], v[12:13], v[116:117] op_sel_hi:[0,1,1]
	v_pk_mul_f32 v[12:13], v[38:39], v[8:9] op_sel_hi:[1,0]
	v_pk_mul_f32 v[118:119], v[4:5], v[118:119] op_sel_hi:[0,1]
	v_pk_fma_f32 v[118:119], v[6:7], v[12:13], v[118:119] op_sel_hi:[0,1,1]
	global_store_dwordx4 v[160:161], v[116:119], off offset:288
	v_pk_mul_f32 v[12:13], v[40:41], v[8:9] op_sel_hi:[1,0]
	s_waitcnt vmcnt(15)
	v_pk_mul_f32 v[120:121], v[4:5], v[120:121] op_sel_hi:[0,1]
	v_pk_fma_f32 v[120:121], v[6:7], v[12:13], v[120:121] op_sel_hi:[0,1,1]
	v_pk_mul_f32 v[12:13], v[42:43], v[8:9] op_sel_hi:[1,0]
	v_pk_mul_f32 v[122:123], v[4:5], v[122:123] op_sel_hi:[0,1]
	v_pk_fma_f32 v[122:123], v[6:7], v[12:13], v[122:123] op_sel_hi:[0,1,1]
	global_store_dwordx4 v[160:161], v[120:123], off offset:320
	v_pk_mul_f32 v[12:13], v[44:45], v[8:9] op_sel_hi:[1,0]
	s_waitcnt vmcnt(15)
	v_pk_mul_f32 v[124:125], v[4:5], v[124:125] op_sel_hi:[0,1]
	v_pk_fma_f32 v[124:125], v[6:7], v[12:13], v[124:125] op_sel_hi:[0,1,1]
	v_pk_mul_f32 v[12:13], v[46:47], v[8:9] op_sel_hi:[1,0]
	v_pk_mul_f32 v[126:127], v[4:5], v[126:127] op_sel_hi:[0,1]
	v_pk_fma_f32 v[126:127], v[6:7], v[12:13], v[126:127] op_sel_hi:[0,1,1]
	global_store_dwordx4 v[160:161], v[124:127], off offset:352
	v_pk_mul_f32 v[12:13], v[16:17], v[8:9] op_sel_hi:[1,0]
	s_waitcnt vmcnt(15)
	v_pk_mul_f32 v[228:229], v[4:5], v[228:229] op_sel_hi:[0,1]
	v_pk_fma_f32 v[228:229], v[6:7], v[12:13], v[228:229] op_sel_hi:[0,1,1]
	v_pk_mul_f32 v[12:13], v[18:19], v[8:9] op_sel_hi:[1,0]
	v_pk_mul_f32 v[230:231], v[4:5], v[230:231] op_sel_hi:[0,1]
	v_pk_fma_f32 v[230:231], v[6:7], v[12:13], v[230:231] op_sel_hi:[0,1,1]
	global_store_dwordx4 v[160:161], v[228:231], off offset:384
	v_pk_mul_f32 v[12:13], v[20:21], v[8:9] op_sel_hi:[1,0]
	s_waitcnt vmcnt(15)
	v_pk_mul_f32 v[232:233], v[4:5], v[232:233] op_sel_hi:[0,1]
	v_pk_fma_f32 v[232:233], v[6:7], v[12:13], v[232:233] op_sel_hi:[0,1,1]
	v_pk_mul_f32 v[12:13], v[22:23], v[8:9] op_sel_hi:[1,0]
	v_pk_mul_f32 v[234:235], v[4:5], v[234:235] op_sel_hi:[0,1]
	v_pk_fma_f32 v[234:235], v[6:7], v[12:13], v[234:235] op_sel_hi:[0,1,1]
	global_store_dwordx4 v[160:161], v[232:235], off offset:416
	v_pk_mul_f32 v[12:13], v[24:25], v[8:9] op_sel_hi:[1,0]
	s_waitcnt vmcnt(15)
	v_pk_mul_f32 v[236:237], v[4:5], v[236:237] op_sel_hi:[0,1]
	v_pk_fma_f32 v[236:237], v[6:7], v[12:13], v[236:237] op_sel_hi:[0,1,1]
	v_pk_mul_f32 v[12:13], v[26:27], v[8:9] op_sel_hi:[1,0]
	v_pk_mul_f32 v[238:239], v[4:5], v[238:239] op_sel_hi:[0,1]
	v_pk_fma_f32 v[238:239], v[6:7], v[12:13], v[238:239] op_sel_hi:[0,1,1]
	global_store_dwordx4 v[160:161], v[236:239], off offset:448
	v_pk_mul_f32 v[12:13], v[28:29], v[8:9] op_sel_hi:[1,0]
	v_pk_mul_f32 v[8:9], v[30:31], v[8:9] op_sel_hi:[1,0]
	s_waitcnt vmcnt(15)
	v_pk_mul_f32 v[240:241], v[4:5], v[240:241] op_sel_hi:[0,1]
	v_pk_mul_f32 v[242:243], v[4:5], v[242:243] op_sel_hi:[0,1]
	v_pk_fma_f32 v[240:241], v[6:7], v[12:13], v[240:241] op_sel_hi:[0,1,1]
	v_pk_fma_f32 v[242:243], v[6:7], v[8:9], v[242:243] op_sel_hi:[0,1,1]
	global_store_dwordx4 v[160:161], v[240:243], off offset:480
	s_nop 1
	v_lshl_add_u64 v[0:1], s[74:75], 0, v[168:169]
	global_load_lds_dwordx4 v[0:1], off
	v_lshl_add_u64 v[0:1], vcc, 0, v[176:177]
	s_mov_b32 m0, s67
	v_readlane_b32 s67, v255, 26
	global_load_lds_dwordx4 v[0:1], off
	v_lshl_add_u64 v[0:1], s[74:75], 0, v[178:179]
	s_mov_b32 m0, s67
	v_readlane_b32 s67, v255, 27
	global_load_lds_dwordx4 v[0:1], off
	v_lshl_add_u64 v[0:1], vcc, 0, v[180:181]
	s_mov_b32 m0, s67
	s_cselect_b64 s[74:75], -1, 0
	global_load_lds_dwordx4 v[0:1], off
	s_and_b64 vcc, exec, s[74:75]
	s_cbranch_vccnz .LBB0_882
	s_mul_i32 s67, s84, 0xc8000
	v_readlane_b32 s68, v255, 13
	s_add_u32 s78, s68, s67
	v_readlane_b32 s67, v255, 14
	s_addc_u32 s79, s67, 0
	s_lshl_b64 s[80:81], s[84:85], 7
	v_readlane_b32 s67, v255, 15
	s_add_u32 s80, s67, s80
	v_readlane_b32 s67, v255, 16
	s_addc_u32 s81, s67, s81
	v_lshl_add_u64 v[0:1], s[78:79], 0, v[168:169]
	s_add_i32 m0, s69, 0x8000
	v_readlane_b32 s67, v254, 57
	global_load_lds_dwordx4 v[0:1], off
	v_lshl_add_u64 v[0:1], s[80:81], 0, v[176:177]
	s_add_i32 m0, s69, 0xc000
	s_nop 0
	global_load_lds_dwordx4 v[0:1], off
	v_lshl_add_u64 v[0:1], s[78:79], 0, v[178:179]
	s_mov_b32 m0, s67
	v_readlane_b32 s67, v254, 58
	global_load_lds_dwordx4 v[0:1], off
	v_lshl_add_u64 v[0:1], s[80:81], 0, v[180:181]
	s_mov_b32 m0, s67
	s_nop 0
	global_load_lds_dwordx4 v[0:1], off
